# grid barrier: last XCD leader bumps every XCC release word directly, leaders spin on their own XCC word (one relay hop removed per barrier)
# speedup vs baseline: 1.0086x; 1.0086x over previous
.LBB0_95:
	s_or_b64 exec, exec, s[8:9]
	v_cvt_f32_u32_e32 v3, v0
	s_waitcnt vmcnt(0)
	v_readfirstlane_b32 s6, v2
	s_add_u32 s8, s4, 0x2400
	s_addc_u32 s9, s5, 0
	v_rcp_iflag_f32_e32 v3, v3
	v_add_u32_e32 v1, s6, v1
	v_add_u32_e32 v4, 1, v1
	s_mov_b64 s[10:11], -1
	v_mul_f32_e32 v2, 0x4f7ffffe, v3
	v_cvt_u32_f32_e32 v2, v2
	v_sub_u32_e32 v3, 0, v0
	v_mul_lo_u32 v3, v3, v2
	v_mul_hi_u32 v3, v2, v3
	v_add_u32_e32 v2, v2, v3
	v_mul_hi_u32 v2, v1, v2
	v_mul_lo_u32 v3, v2, v0
	v_sub_u32_e32 v1, v1, v3
	v_add_u32_e32 v5, 1, v2
	v_cmp_ge_u32_e32 vcc, v1, v0
	v_sub_u32_e32 v3, v1, v0
	s_nop 0
	v_cndmask_b32_e32 v2, v2, v5, vcc
	v_cndmask_b32_e32 v1, v1, v3, vcc
	v_add_u32_e32 v3, 1, v2
	v_cmp_ge_u32_e32 vcc, v1, v0
	s_nop 1
	v_cndmask_b32_e32 v2, v2, v3, vcc
	v_mul_lo_u32 v1, v0, v2
	v_add_u32_e32 v0, v1, v0
	v_cmp_ne_u32_e32 vcc, v4, v0
	v_mov_b64_e32 v[0:1], s[8:9]
	s_and_saveexec_b64 s[6:7], vcc
	s_cbranch_execz .Lxbrel_0
	v_mov_b32_e32 v0, 0
	global_load_dword v1, v0, s[8:9] sc1
	s_mov_b64 s[14:15], 0
	s_waitcnt vmcnt(0)
	v_cmp_eq_u32_e32 vcc, v1, v2
	s_and_saveexec_b64 s[12:13], vcc
	s_cbranch_execz .LBB0_106
	s_add_u32 s10, s88, 0x80200
	s_addc_u32 s11, s89, 0
	s_mov_b32 s24, 1
	s_branch .LBB0_99

.LBB0_106:
	s_or_b64 exec, exec, s[12:13]
	v_mov_b64_e32 v[0:1], s[10:11]
	s_orn2_b64 s[10:11], s[14:15], exec
	s_branch .LBB0_107
.Lxbrel_0:
	s_mov_b64 exec, s[6:7]
	s_mov_b64 s[10:11], 0
	v_mov_b32_e32 v2, 1
	v_mov_b32_e32 v3, 0x82400
	global_atomic_add v3, v2, s[88:89]
	global_atomic_add v3, v2, s[88:89] offset:256
	global_atomic_add v3, v2, s[88:89] offset:512
	global_atomic_add v3, v2, s[88:89] offset:768
	global_atomic_add v3, v2, s[88:89] offset:1024
	global_atomic_add v3, v2, s[88:89] offset:1280
	global_atomic_add v3, v2, s[88:89] offset:1536
	global_atomic_add v3, v2, s[88:89] offset:1792
	global_atomic_add v3, v2, s[88:89] offset:2048
	global_atomic_add v3, v2, s[88:89] offset:2304
	global_atomic_add v3, v2, s[88:89] offset:2560
	global_atomic_add v3, v2, s[88:89] offset:2816
	global_atomic_add v3, v2, s[88:89] offset:3072
	global_atomic_add v3, v2, s[88:89] offset:3328
	global_atomic_add v3, v2, s[88:89] offset:3584
	global_atomic_add v3, v2, s[88:89] offset:3840

.LBB0_109:
	s_or_b64 exec, exec, s[6:7]
	s_mov_b64 s[6:7], exec
	v_mbcnt_lo_u32_b32 v0, s6, 0
	v_mbcnt_hi_u32_b32 v0, s7, v0
	v_cmp_eq_u32_e32 vcc, 0, v0
	s_waitcnt vmcnt(0)
	buffer_inv sc1
	s_and_saveexec_b64 s[8:9], vcc
	s_cbranch_execz .LBB0_111
	s_bcnt1_i32_b64 s6, s[6:7]
	v_mov_b32_e32 v0, 0x2000
	v_mov_b32_e32 v1, s6
.LBB0_111:
	s_or_b64 exec, exec, s[8:9]
	s_waitcnt vmcnt(0)

.LBB0_166:
	s_or_b64 exec, exec, s[10:11]
	v_cvt_f32_u32_e32 v3, v0
	s_waitcnt vmcnt(0)
	v_readfirstlane_b32 s8, v2
	s_add_u32 s10, s6, 0x2400
	s_addc_u32 s11, s7, 0
	v_rcp_iflag_f32_e32 v3, v3
	v_add_u32_e32 v1, s8, v1
	v_add_u32_e32 v4, 1, v1
	s_mov_b64 s[12:13], -1
	v_mul_f32_e32 v2, 0x4f7ffffe, v3
	v_cvt_u32_f32_e32 v2, v2
	v_sub_u32_e32 v3, 0, v0
	v_mul_lo_u32 v3, v3, v2
	v_mul_hi_u32 v3, v2, v3
	v_add_u32_e32 v2, v2, v3
	v_mul_hi_u32 v2, v1, v2
	v_mul_lo_u32 v3, v2, v0
	v_sub_u32_e32 v1, v1, v3
	v_add_u32_e32 v5, 1, v2
	v_cmp_ge_u32_e32 vcc, v1, v0
	v_sub_u32_e32 v3, v1, v0
	s_nop 0
	v_cndmask_b32_e32 v2, v2, v5, vcc
	v_cndmask_b32_e32 v1, v1, v3, vcc
	v_add_u32_e32 v3, 1, v2
	v_cmp_ge_u32_e32 vcc, v1, v0
	s_nop 1
	v_cndmask_b32_e32 v2, v2, v3, vcc
	v_mul_lo_u32 v1, v0, v2
	v_add_u32_e32 v0, v1, v0
	v_cmp_ne_u32_e32 vcc, v4, v0
	v_mov_b64_e32 v[0:1], s[10:11]
	s_and_saveexec_b64 s[8:9], vcc
	s_cbranch_execz .Lxbrel_1
	v_mov_b32_e32 v0, 0
	global_load_dword v1, v0, s[10:11] sc1
	s_mov_b64 s[16:17], 0
	s_waitcnt vmcnt(0)
	v_cmp_eq_u32_e32 vcc, v1, v2
	s_and_saveexec_b64 s[14:15], vcc
	s_cbranch_execz .LBB0_177
	s_add_u32 s12, s88, 0x80200
	s_addc_u32 s13, s89, 0
	s_mov_b32 s26, 1
	s_branch .LBB0_170

.LBB0_177:
	s_or_b64 exec, exec, s[14:15]
	v_mov_b64_e32 v[0:1], s[12:13]
	s_orn2_b64 s[12:13], s[16:17], exec
	s_branch .LBB0_178
.Lxbrel_1:
	s_mov_b64 exec, s[8:9]
	s_mov_b64 s[12:13], 0
	v_mov_b32_e32 v2, 1
	v_mov_b32_e32 v3, 0x82400
	global_atomic_add v3, v2, s[88:89]
	global_atomic_add v3, v2, s[88:89] offset:256
	global_atomic_add v3, v2, s[88:89] offset:512
	global_atomic_add v3, v2, s[88:89] offset:768
	global_atomic_add v3, v2, s[88:89] offset:1024
	global_atomic_add v3, v2, s[88:89] offset:1280
	global_atomic_add v3, v2, s[88:89] offset:1536
	global_atomic_add v3, v2, s[88:89] offset:1792
	global_atomic_add v3, v2, s[88:89] offset:2048
	global_atomic_add v3, v2, s[88:89] offset:2304
	global_atomic_add v3, v2, s[88:89] offset:2560
	global_atomic_add v3, v2, s[88:89] offset:2816
	global_atomic_add v3, v2, s[88:89] offset:3072
	global_atomic_add v3, v2, s[88:89] offset:3328
	global_atomic_add v3, v2, s[88:89] offset:3584
	global_atomic_add v3, v2, s[88:89] offset:3840

.LBB0_180:
	s_or_b64 exec, exec, s[8:9]
	s_mov_b64 s[8:9], exec
	v_mbcnt_lo_u32_b32 v0, s8, 0
	v_mbcnt_hi_u32_b32 v0, s9, v0
	v_cmp_eq_u32_e32 vcc, 0, v0
	s_waitcnt vmcnt(0)
	buffer_inv sc1
	s_and_saveexec_b64 s[10:11], vcc
	s_cbranch_execz .LBB0_182
	s_bcnt1_i32_b64 s8, s[8:9]
	v_mov_b32_e32 v0, 0x2000
	v_mov_b32_e32 v1, s8
.LBB0_182:
	s_or_b64 exec, exec, s[10:11]
	s_waitcnt vmcnt(0)

.LBB0_397:
	s_or_b64 exec, exec, s[6:7]
	s_mov_b64 s[6:7], exec
	v_mbcnt_lo_u32_b32 v0, s6, 0
	v_mbcnt_hi_u32_b32 v0, s7, v0
	v_cmp_eq_u32_e32 vcc, 0, v0
	s_waitcnt vmcnt(0)
	buffer_inv sc1
	s_and_saveexec_b64 s[8:9], vcc
	s_cbranch_execz .LBB0_399
	s_bcnt1_i32_b64 s6, s[6:7]
	v_mov_b32_e32 v0, 0x2000
	v_mov_b32_e32 v1, s6
.LBB0_399:
	s_or_b64 exec, exec, s[8:9]
	s_waitcnt vmcnt(0)

.LBB0_506:
	s_or_b64 exec, exec, s[6:7]
	s_mov_b64 s[6:7], exec
	v_mbcnt_lo_u32_b32 v0, s6, 0
	v_mbcnt_hi_u32_b32 v0, s7, v0
	v_cmp_eq_u32_e32 vcc, 0, v0
	s_waitcnt vmcnt(0)
	buffer_inv sc1
	s_and_saveexec_b64 s[8:9], vcc
	s_cbranch_execz .LBB0_508
	s_bcnt1_i32_b64 s6, s[6:7]
	v_mov_b32_e32 v0, 0x2000
	v_mov_b32_e32 v1, s6
.LBB0_508:
	s_or_b64 exec, exec, s[8:9]
	s_waitcnt vmcnt(0)

.LBB0_568:
	s_or_b64 exec, exec, s[6:7]
	s_mov_b64 s[6:7], exec
	v_mbcnt_lo_u32_b32 v0, s6, 0
	v_mbcnt_hi_u32_b32 v0, s7, v0
	v_cmp_eq_u32_e32 vcc, 0, v0
	s_waitcnt vmcnt(0)
	buffer_inv sc1
	s_and_saveexec_b64 s[8:9], vcc
	s_cbranch_execz .LBB0_570
	s_bcnt1_i32_b64 s6, s[6:7]
	v_mov_b32_e32 v0, 0x2000
	v_mov_b32_e32 v1, s6
.LBB0_570:
	s_or_b64 exec, exec, s[8:9]
	s_waitcnt vmcnt(0)

.LBB0_634:
	s_or_b64 exec, exec, s[8:9]
	v_cvt_f32_u32_e32 v3, v0
	s_waitcnt vmcnt(0)
	v_readfirstlane_b32 s6, v2
	s_add_u32 s8, s4, 0x2400
	s_addc_u32 s9, s5, 0
	v_rcp_iflag_f32_e32 v3, v3
	v_add_u32_e32 v1, s6, v1
	v_add_u32_e32 v4, 1, v1
	s_mov_b64 s[12:13], -1
	v_mul_f32_e32 v2, 0x4f7ffffe, v3
	v_cvt_u32_f32_e32 v2, v2
	v_sub_u32_e32 v3, 0, v0
	v_mul_lo_u32 v3, v3, v2
	v_mul_hi_u32 v3, v2, v3
	v_add_u32_e32 v2, v2, v3
	v_mul_hi_u32 v2, v1, v2
	v_mul_lo_u32 v3, v2, v0
	v_sub_u32_e32 v1, v1, v3
	v_add_u32_e32 v5, 1, v2
	v_cmp_ge_u32_e32 vcc, v1, v0
	v_sub_u32_e32 v3, v1, v0
	s_nop 0
	v_cndmask_b32_e32 v2, v2, v5, vcc
	v_cndmask_b32_e32 v1, v1, v3, vcc
	v_add_u32_e32 v3, 1, v2
	v_cmp_ge_u32_e32 vcc, v1, v0
	s_nop 1
	v_cndmask_b32_e32 v2, v2, v3, vcc
	v_mul_lo_u32 v1, v0, v2
	v_add_u32_e32 v0, v1, v0
	v_cmp_ne_u32_e32 vcc, v4, v0
	v_mov_b64_e32 v[0:1], s[8:9]
	s_and_saveexec_b64 s[6:7], vcc
	s_cbranch_execz .Lxbrel_5
	v_mov_b32_e32 v0, 0
	global_load_dword v1, v0, s[8:9] sc1
	s_mov_b64 s[16:17], 0
	s_waitcnt vmcnt(0)
	v_cmp_eq_u32_e32 vcc, v1, v2
	s_and_saveexec_b64 s[14:15], vcc
	s_cbranch_execz .LBB0_645
	s_add_u32 s12, s88, 0x80200
	s_addc_u32 s13, s89, 0
	s_mov_b32 s26, 1
	s_branch .LBB0_638

.Lxbrel_5:
	s_mov_b64 exec, s[6:7]
	s_mov_b64 s[12:13], 0
	v_mov_b32_e32 v2, 1
	v_mov_b32_e32 v3, 0x82400
	global_atomic_add v3, v2, s[88:89]
	global_atomic_add v3, v2, s[88:89] offset:256
	global_atomic_add v3, v2, s[88:89] offset:512
	global_atomic_add v3, v2, s[88:89] offset:768
	global_atomic_add v3, v2, s[88:89] offset:1024
	global_atomic_add v3, v2, s[88:89] offset:1280
	global_atomic_add v3, v2, s[88:89] offset:1536
	global_atomic_add v3, v2, s[88:89] offset:1792
	global_atomic_add v3, v2, s[88:89] offset:2048
	global_atomic_add v3, v2, s[88:89] offset:2304
	global_atomic_add v3, v2, s[88:89] offset:2560
	global_atomic_add v3, v2, s[88:89] offset:2816
	global_atomic_add v3, v2, s[88:89] offset:3072
	global_atomic_add v3, v2, s[88:89] offset:3328
	global_atomic_add v3, v2, s[88:89] offset:3584
	global_atomic_add v3, v2, s[88:89] offset:3840

.LBB0_648:
	s_or_b64 exec, exec, s[6:7]
	s_mov_b64 s[6:7], exec
	v_mbcnt_lo_u32_b32 v0, s6, 0
	v_mbcnt_hi_u32_b32 v0, s7, v0
	v_cmp_eq_u32_e32 vcc, 0, v0
	s_waitcnt vmcnt(0)
	buffer_inv sc1
	s_and_saveexec_b64 s[8:9], vcc
	s_cbranch_execz .LBB0_650
	s_bcnt1_i32_b64 s6, s[6:7]
	v_mov_b32_e32 v0, 0x2000
	v_mov_b32_e32 v1, s6
.LBB0_650:
	s_or_b64 exec, exec, s[8:9]
	s_waitcnt vmcnt(0)

.LBB0_699:
	s_or_b64 exec, exec, s[8:9]
	v_cvt_f32_u32_e32 v3, v0
	s_waitcnt vmcnt(0)
	v_readfirstlane_b32 s6, v2
	s_add_u32 s8, s4, 0x2400
	s_addc_u32 s9, s5, 0
	v_rcp_iflag_f32_e32 v3, v3
	v_add_u32_e32 v1, s6, v1
	v_add_u32_e32 v4, 1, v1
	s_mov_b64 s[10:11], -1
	v_mul_f32_e32 v2, 0x4f7ffffe, v3
	v_cvt_u32_f32_e32 v2, v2
	v_sub_u32_e32 v3, 0, v0
	v_mul_lo_u32 v3, v3, v2
	v_mul_hi_u32 v3, v2, v3
	v_add_u32_e32 v2, v2, v3
	v_mul_hi_u32 v2, v1, v2
	v_mul_lo_u32 v3, v2, v0
	v_sub_u32_e32 v1, v1, v3
	v_add_u32_e32 v5, 1, v2
	v_cmp_ge_u32_e32 vcc, v1, v0
	v_sub_u32_e32 v3, v1, v0
	s_nop 0
	v_cndmask_b32_e32 v2, v2, v5, vcc
	v_cndmask_b32_e32 v1, v1, v3, vcc
	v_add_u32_e32 v3, 1, v2
	v_cmp_ge_u32_e32 vcc, v1, v0
	s_nop 1
	v_cndmask_b32_e32 v2, v2, v3, vcc
	v_mul_lo_u32 v1, v0, v2
	v_add_u32_e32 v0, v1, v0
	v_cmp_ne_u32_e32 vcc, v4, v0
	v_mov_b64_e32 v[0:1], s[8:9]
	s_and_saveexec_b64 s[6:7], vcc
	s_cbranch_execz .Lxbrel_6
	v_mov_b32_e32 v0, 0
	global_load_dword v1, v0, s[8:9] sc1
	s_mov_b64 s[16:17], 0
	s_waitcnt vmcnt(0)
	v_cmp_eq_u32_e32 vcc, v1, v2
	s_and_saveexec_b64 s[14:15], vcc
	s_cbranch_execz .LBB0_710
	s_add_u32 s10, s88, 0x80200
	s_addc_u32 s11, s89, 0
	s_mov_b32 s26, 1
	s_branch .LBB0_703

.LBB0_710:
	s_or_b64 exec, exec, s[14:15]
	v_mov_b64_e32 v[0:1], s[10:11]
	s_orn2_b64 s[10:11], s[16:17], exec
	s_branch .LBB0_711

.LBB0_713:
	s_or_b64 exec, exec, s[6:7]
	s_mov_b64 s[6:7], exec
	v_mbcnt_lo_u32_b32 v0, s6, 0
	v_mbcnt_hi_u32_b32 v0, s7, v0
	v_cmp_eq_u32_e32 vcc, 0, v0
	s_waitcnt vmcnt(0)
	buffer_inv sc1
	s_and_saveexec_b64 s[8:9], vcc
	s_cbranch_execz .LBB0_715
	s_bcnt1_i32_b64 s6, s[6:7]
	v_mov_b32_e32 v0, 0x2000
	v_mov_b32_e32 v1, s6
.LBB0_715:
	s_or_b64 exec, exec, s[8:9]
	s_waitcnt vmcnt(0)

.LBB0_779:
	s_or_b64 exec, exec, s[10:11]
	v_cvt_f32_u32_e32 v3, v0
	s_waitcnt vmcnt(0)
	v_readfirstlane_b32 s8, v2
	s_add_u32 s10, s4, 0x2400
	s_addc_u32 s11, s5, 0
	v_rcp_iflag_f32_e32 v3, v3
	v_add_u32_e32 v1, s8, v1
	v_add_u32_e32 v4, 1, v1
	s_mov_b64 s[12:13], -1
	v_mul_f32_e32 v2, 0x4f7ffffe, v3
	v_cvt_u32_f32_e32 v2, v2
	v_sub_u32_e32 v3, 0, v0
	v_mul_lo_u32 v3, v3, v2
	v_mul_hi_u32 v3, v2, v3
	v_add_u32_e32 v2, v2, v3
	v_mul_hi_u32 v2, v1, v2
	v_mul_lo_u32 v3, v2, v0
	v_sub_u32_e32 v1, v1, v3
	v_add_u32_e32 v5, 1, v2
	v_cmp_ge_u32_e32 vcc, v1, v0
	v_sub_u32_e32 v3, v1, v0
	s_nop 0
	v_cndmask_b32_e32 v2, v2, v5, vcc
	v_cndmask_b32_e32 v1, v1, v3, vcc
	v_add_u32_e32 v3, 1, v2
	v_cmp_ge_u32_e32 vcc, v1, v0
	s_nop 1
	v_cndmask_b32_e32 v2, v2, v3, vcc
	v_mul_lo_u32 v1, v0, v2
	v_add_u32_e32 v0, v1, v0
	v_cmp_ne_u32_e32 vcc, v4, v0
	v_mov_b64_e32 v[0:1], s[10:11]
	s_and_saveexec_b64 s[8:9], vcc
	s_cbranch_execz .Lxbrel_7
	v_mov_b32_e32 v0, 0
	global_load_dword v1, v0, s[10:11] sc1
	s_mov_b64 s[16:17], 0
	s_waitcnt vmcnt(0)
	v_cmp_eq_u32_e32 vcc, v1, v2
	s_and_saveexec_b64 s[14:15], vcc
	s_cbranch_execz .LBB0_790
	s_add_u32 s12, s88, 0x80200
	s_addc_u32 s13, s89, 0
	s_mov_b32 s26, 1
	s_branch .LBB0_783

.LBB0_793:
	s_or_b64 exec, exec, s[8:9]
	s_mov_b64 s[8:9], exec
	v_mbcnt_lo_u32_b32 v0, s8, 0
	v_mbcnt_hi_u32_b32 v0, s9, v0
	v_cmp_eq_u32_e32 vcc, 0, v0
	s_waitcnt vmcnt(0)
	buffer_inv sc1
	s_and_saveexec_b64 s[10:11], vcc
	s_cbranch_execz .LBB0_795
	s_bcnt1_i32_b64 s8, s[8:9]
	v_mov_b32_e32 v0, 0x2000
	v_mov_b32_e32 v1, s8
.LBB0_795:
	s_or_b64 exec, exec, s[10:11]
	s_waitcnt vmcnt(0)

.LBB0_913:
	s_or_b64 exec, exec, s[8:9]
	s_mov_b64 s[8:9], exec
	v_mbcnt_lo_u32_b32 v0, s8, 0
	v_mbcnt_hi_u32_b32 v0, s9, v0
	v_cmp_eq_u32_e32 vcc, 0, v0
	s_waitcnt vmcnt(0)
	buffer_inv sc1
	s_and_saveexec_b64 s[10:11], vcc
	s_cbranch_execz .LBB0_915
	s_bcnt1_i32_b64 s8, s[8:9]
	v_mov_b32_e32 v0, 0x2000
	v_mov_b32_e32 v1, s8
.LBB0_915:
	s_or_b64 exec, exec, s[10:11]
	s_waitcnt vmcnt(0)

.LBB0_1009:
	s_or_b64 exec, exec, s[6:7]
	s_mov_b64 s[6:7], exec
	v_mbcnt_lo_u32_b32 v0, s6, 0
	v_mbcnt_hi_u32_b32 v0, s7, v0
	v_cmp_eq_u32_e32 vcc, 0, v0
	s_waitcnt vmcnt(0)
	buffer_inv sc1
	s_and_saveexec_b64 s[8:9], vcc
	s_cbranch_execz .LBB0_1011
	s_bcnt1_i32_b64 s6, s[6:7]
	v_mov_b32_e32 v0, 0x2000
	v_mov_b32_e32 v1, s6
.LBB0_1011:
	s_or_b64 exec, exec, s[8:9]
	s_waitcnt vmcnt(0)

.LBB0_1069:
	s_or_b64 exec, exec, s[6:7]
	s_mov_b64 s[6:7], exec
	v_mbcnt_lo_u32_b32 v0, s6, 0
	v_mbcnt_hi_u32_b32 v0, s7, v0
	v_cmp_eq_u32_e32 vcc, 0, v0
	s_waitcnt vmcnt(0)
	buffer_inv sc1
	s_and_saveexec_b64 s[8:9], vcc
	s_cbranch_execz .LBB0_1071
	s_bcnt1_i32_b64 s6, s[6:7]
	v_mov_b32_e32 v0, 0x2000
	v_mov_b32_e32 v1, s6
.LBB0_1071:
	s_or_b64 exec, exec, s[8:9]
	s_waitcnt vmcnt(0)

.LBB0_1162:
	s_or_b64 exec, exec, s[8:9]
	s_mov_b64 s[8:9], exec
	v_mbcnt_lo_u32_b32 v0, s8, 0
	v_mbcnt_hi_u32_b32 v0, s9, v0
	v_cmp_eq_u32_e32 vcc, 0, v0
	s_waitcnt vmcnt(0)
	buffer_inv sc1
	s_and_saveexec_b64 s[10:11], vcc
	s_cbranch_execz .LBB0_1164
	s_bcnt1_i32_b64 s8, s[8:9]
	v_mov_b32_e32 v0, 0x2000
	v_mov_b32_e32 v1, s8
.LBB0_1164:
	s_or_b64 exec, exec, s[10:11]
	s_waitcnt vmcnt(0)
